# grid barrier: L1 invalidate issued by wave 1 at arrival (overlaps the wait) + sc1 16B stores
# speedup vs baseline: 1.0191x; 1.0104x over previous
.LBB0_82:
	s_or_b64 exec, exec, s[0:1]
	s_cmp_lt_i32 s26, 2
	s_cbranch_scc1 .LBB0_136
	s_getreg_b32 s2, hwreg(HW_REG_XCC_ID, 0, 4)
	v_readlane_b32 s0, v250, 4
	v_mov_b32 v1, s0
	s_waitcnt vmcnt(0)
	s_waitcnt lgkmcnt(0)
	s_barrier
	s_cmp_eq_u32 s43, 1
	s_cbranch_scc0 .Learlyinv_0
	buffer_inv sc1
	s_waitcnt vmcnt(0)
.Learlyinv_0:
	s_mov_b64 s[0:1], exec
	v_readlane_b32 s4, v250, 2
	v_readlane_b32 s5, v250, 3
	s_and_b64 s[4:5], s[0:1], s[4:5]
	s_mov_b64 exec, s[4:5]
	s_cbranch_execz .LBB0_135
	s_waitcnt vmcnt(0) expcnt(0) lgkmcnt(0)
	ds_read_b32 v2, v1
	ds_read_b32 v0, v1 offset:4
	s_and_b32 s18, s2, 15
	s_waitcnt lgkmcnt(1)
	v_cmp_eq_u32_e32 vcc, 0, v2
	s_and_saveexec_b64 s[2:3], vcc
	s_cbranch_execz .LBB0_99
	v_readlane_b32 s4, v250, 0
	v_readlane_b32 s5, v250, 1
	s_load_dwordx2 s[8:9], s[4:5], 0x4
	s_add_u32 s4, s60, 0x1000
	s_addc_u32 s5, s61, 0
	s_add_u32 s6, s60, 0x1100
	s_addc_u32 s7, s61, 0
	s_waitcnt lgkmcnt(0)
	s_mul_i32 s19, s8, s37
	s_add_u32 s8, s60, 0x1200
	s_mul_i32 s19, s19, s9
	s_addc_u32 s9, s61, 0
	s_add_u32 s10, s60, 0x1300
	s_addc_u32 s11, s61, 0
	s_mov_b32 s20, 1
	v_mov_b32_e32 v17, 0
	s_branch .LBB0_87

.LBB0_114:
	s_or_b64 exec, exec, s[6:7]
	s_waitcnt vmcnt(0)
	s_waitcnt vmcnt(0)

.LBB0_132:
	s_or_b64 exec, exec, s[4:5]
	s_mov_b64 s[4:5], exec
	v_mbcnt_lo_u32_b32 v0, s4, 0
	v_mbcnt_hi_u32_b32 v0, s5, v0
	v_cmp_eq_u32_e32 vcc, 0, v0
	s_waitcnt vmcnt(0)
	s_and_saveexec_b64 s[6:7], vcc
	s_cbranch_execz .LBB0_134
	s_bcnt1_i32_b64 s4, s[4:5]
	v_mov_b32_e32 v0, 0x2000
	v_mov_b32_e32 v1, s4
	global_atomic_add v0, v1, s[2:3] offset:1024

.LBB0_163:
	s_cmp_lt_i32 s26, 3
	s_cbranch_scc1 .LBB0_217
	s_getreg_b32 s2, hwreg(HW_REG_XCC_ID, 0, 4)
	v_readlane_b32 s0, v250, 4
	v_mov_b32 v1, s0
	s_waitcnt vmcnt(0)
	s_barrier
	s_cmp_eq_u32 s43, 1
	s_cbranch_scc0 .Learlyinv_1
	buffer_inv sc1
	s_waitcnt vmcnt(0)

.LBB0_282:
	s_cmp_lt_i32 s29, 4
	s_cbranch_scc1 .LBB0_336
	s_getreg_b32 s2, hwreg(HW_REG_XCC_ID, 0, 4)
	v_readlane_b32 s0, v250, 4
	s_waitcnt vmcnt(0)
	v_mov_b32 v1, s0
	s_waitcnt vmcnt(0)
	s_barrier
	s_cmp_eq_u32 s43, 1
	s_cbranch_scc0 .Learlyinv_2
	buffer_inv sc1
	s_waitcnt vmcnt(0)

.LBB0_452:
	v_readlane_b32 s0, v255, 35
	s_add_i32 s22, s0, 4
	s_cmp_ge_i32 s22, s1
	s_cbranch_scc1 .LBB0_506
	s_getreg_b32 s1, hwreg(HW_REG_XCC_ID, 0, 4)
	v_readlane_b32 s0, v250, 4
	s_waitcnt vmcnt(3)
	v_mov_b32 v1, s0
	s_waitcnt vmcnt(0)
	s_waitcnt lgkmcnt(0)
	s_barrier
	s_cmp_eq_u32 s43, 1
	s_cbranch_scc0 .Learlyinv_3
	buffer_inv sc1
	s_waitcnt vmcnt(0)
.Learlyinv_3:
	s_mov_b64 s[4:5], exec
	v_readlane_b32 s2, v250, 2
	v_readlane_b32 s3, v250, 3
	s_and_b64 s[2:3], s[4:5], s[2:3]
	s_mov_b64 exec, s[2:3]
	s_cbranch_execz .LBB0_505
	s_waitcnt vmcnt(0) expcnt(0) lgkmcnt(0)
	ds_read_b32 v2, v1
	ds_read_b32 v0, v1 offset:4
	s_and_b32 s1, s1, 15
	s_waitcnt lgkmcnt(1)
	v_cmp_eq_u32_e32 vcc, 0, v2
	s_and_saveexec_b64 s[6:7], vcc
	s_cbranch_execz .LBB0_469
	v_readlane_b32 s8, v250, 0
	v_readlane_b32 s9, v250, 1
	s_load_dwordx2 s[2:3], s[8:9], 0x4
	s_mov_b32 s13, 1
	s_waitcnt lgkmcnt(0)
	s_mul_i32 s12, s2, s37
	s_mul_i32 s12, s12, s3
	s_branch .LBB0_457

.LBB0_484:
	s_or_b64 exec, exec, s[10:11]
	s_waitcnt vmcnt(0)
	s_waitcnt vmcnt(0)

.LBB0_502:
	s_or_b64 exec, exec, s[8:9]
	s_mov_b64 s[2:3], exec
	v_mbcnt_lo_u32_b32 v0, s2, 0
	v_mbcnt_hi_u32_b32 v0, s3, v0
	v_cmp_eq_u32_e32 vcc, 0, v0
	s_waitcnt vmcnt(0)
	s_and_saveexec_b64 s[8:9], vcc
	s_cbranch_execz .LBB0_504
	s_bcnt1_i32_b64 s1, s[2:3]
	v_mov_b32_e32 v0, s1
	v_mov_b32_e32 v1, 0x2000
	global_atomic_add v1, v0, s[6:7] offset:1024

.LBB0_584:
	v_readlane_b32 s0, v255, 35
	s_add_i32 s1, s0, 5
	s_cmp_ge_i32 s1, s57
	s_cbranch_scc1 .LBB0_638
	s_getreg_b32 s2, hwreg(HW_REG_XCC_ID, 0, 4)
	v_readlane_b32 s0, v250, 4
	v_mov_b32 v1, s0
	s_waitcnt vmcnt(0)
	s_waitcnt vmcnt(0)
	s_barrier
	s_cmp_eq_u32 s43, 1
	s_cbranch_scc0 .Learlyinv_4
	buffer_inv sc1
	s_waitcnt vmcnt(0)
.Learlyinv_4:
	s_mov_b64 s[4:5], exec
	v_readlane_b32 s6, v250, 2
	v_readlane_b32 s7, v250, 3
	s_and_b64 s[6:7], s[4:5], s[6:7]
	s_mov_b64 exec, s[6:7]
	s_cbranch_execz .LBB0_637
	s_waitcnt vmcnt(0) expcnt(0) lgkmcnt(0)
	ds_read_b32 v2, v1
	ds_read_b32 v0, v1 offset:4
	s_and_b32 s12, s2, 15
	s_waitcnt lgkmcnt(1)
	v_cmp_eq_u32_e32 vcc, 0, v2
	s_and_saveexec_b64 s[6:7], vcc
	s_cbranch_execz .LBB0_601
	v_readlane_b32 s8, v250, 0
	v_readlane_b32 s9, v250, 1
	s_load_dwordx2 s[2:3], s[8:9], 0x4
	s_mov_b32 s14, 1
	s_waitcnt lgkmcnt(0)
	s_mul_i32 s13, s2, s37
	s_mul_i32 s13, s13, s3
	s_branch .LBB0_589

.LBB0_634:
	s_or_b64 exec, exec, s[8:9]
	s_mov_b64 s[2:3], exec
	v_mbcnt_lo_u32_b32 v0, s2, 0
	v_mbcnt_hi_u32_b32 v0, s3, v0
	v_cmp_eq_u32_e32 vcc, 0, v0
	s_waitcnt vmcnt(0)
	s_and_saveexec_b64 s[8:9], vcc
	s_cbranch_execz .LBB0_636
	s_bcnt1_i32_b64 s2, s[2:3]
	v_mov_b32_e32 v0, s2
	v_mov_b32_e32 v1, 0x2000
	global_atomic_add v1, v0, s[6:7] offset:1024

.LBB0_821:
	v_readlane_b32 s0, v255, 35
	s_add_i32 s1, s0, 6
	s_cmp_ge_i32 s1, s65
	s_cbranch_scc1 .LBB0_875
	s_getreg_b32 s2, hwreg(HW_REG_XCC_ID, 0, 4)
	v_readlane_b32 s0, v250, 4
	v_mov_b32 v1, s0
	s_waitcnt vmcnt(0)
	s_waitcnt vmcnt(0) lgkmcnt(0)
	s_barrier
	s_cmp_eq_u32 s43, 1
	s_cbranch_scc0 .Learlyinv_5
	buffer_inv sc1
	s_waitcnt vmcnt(0)
.Learlyinv_5:
	s_mov_b64 s[6:7], exec
	v_readlane_b32 s4, v250, 2
	v_readlane_b32 s5, v250, 3
	s_and_b64 s[4:5], s[6:7], s[4:5]
	s_mov_b64 exec, s[4:5]
	s_cbranch_execz .LBB0_874
	s_waitcnt vmcnt(0) expcnt(0) lgkmcnt(0)
	ds_read_b32 v2, v1
	ds_read_b32 v0, v1 offset:4
	s_and_b32 s12, s2, 15
	s_waitcnt lgkmcnt(1)
	v_cmp_eq_u32_e32 vcc, 0, v2
	s_and_saveexec_b64 s[8:9], vcc
	s_cbranch_execz .LBB0_838
	v_readlane_b32 s4, v250, 0
	v_readlane_b32 s5, v250, 1
	s_load_dwordx2 s[2:3], s[4:5], 0x4
	s_mov_b32 s14, 1
	s_waitcnt lgkmcnt(0)
	s_mul_i32 s13, s2, s37
	s_mul_i32 s13, s13, s3
	s_branch .LBB0_826

.LBB0_871:
	s_or_b64 exec, exec, s[4:5]
	s_mov_b64 s[2:3], exec
	v_mbcnt_lo_u32_b32 v0, s2, 0
	v_mbcnt_hi_u32_b32 v0, s3, v0
	v_cmp_eq_u32_e32 vcc, 0, v0
	s_waitcnt vmcnt(0)
	s_and_saveexec_b64 s[4:5], vcc
	s_cbranch_execz .LBB0_873
	s_bcnt1_i32_b64 s2, s[2:3]
	v_mov_b32_e32 v0, s2
	v_mov_b32_e32 v1, 0x2000
	global_atomic_add v1, v0, s[8:9] offset:1024

.LBB0_997:
	s_or_b64 exec, exec, s[6:7]
	v_readlane_b32 s0, v255, 35
	s_add_i32 s1, s0, 7
	s_cmp_ge_i32 s1, s4
	s_cbranch_scc1 .LBB0_1051
	s_getreg_b32 s2, hwreg(HW_REG_XCC_ID, 0, 4)
	v_readlane_b32 s0, v250, 4
	v_mov_b32 v1, s0
	s_waitcnt vmcnt(0)
	s_barrier
	s_cmp_eq_u32 s43, 1
	s_cbranch_scc0 .Learlyinv_6
	buffer_inv sc1
	s_waitcnt vmcnt(0)

.LBB0_1173:
	v_readlane_b32 s0, v255, 35
	s_add_i32 s1, s0, 8
	s_cmp_ge_i32 s1, s28
	s_cbranch_scc1 .LBB0_1227
	s_getreg_b32 s2, hwreg(HW_REG_XCC_ID, 0, 4)
	v_readlane_b32 s0, v250, 4
	v_mov_b32 v1, s0
	s_waitcnt vmcnt(0)
	s_waitcnt vmcnt(0)
	s_barrier
	s_cmp_eq_u32 s43, 1
	s_cbranch_scc0 .Learlyinv_7
	buffer_inv sc1
	s_waitcnt vmcnt(0)

.LBB0_1233:
	v_readlane_b32 s0, v255, 35
	s_add_i32 s1, s0, 9
	s_cmp_ge_i32 s1, s4
	s_cbranch_scc1 .LBB0_1287
	s_getreg_b32 s2, hwreg(HW_REG_XCC_ID, 0, 4)
	v_readlane_b32 s0, v250, 4
	v_mov_b32 v1, s0
	s_waitcnt vmcnt(0)
	s_waitcnt vmcnt(0)
	s_barrier
	s_cmp_eq_u32 s43, 1
	s_cbranch_scc0 .Learlyinv_8
	buffer_inv sc1
	s_waitcnt vmcnt(0)

.LBB0_1330:
	v_readlane_b32 s0, v255, 35
	s_add_i32 s1, s0, 10
	s_cmp_ge_i32 s1, s25
	s_cbranch_scc1 .LBB0_1384
	s_getreg_b32 s2, hwreg(HW_REG_XCC_ID, 0, 4)
	v_readlane_b32 s0, v250, 4
	v_mov_b32 v1, s0
	s_waitcnt vmcnt(0)
	s_barrier
	s_cmp_eq_u32 s43, 1
	s_cbranch_scc0 .Learlyinv_9
	buffer_inv sc1
	s_waitcnt vmcnt(0)

.LBB0_1449:
	s_or_b64 exec, exec, s[4:5]
	v_readlane_b32 s0, v255, 35
	s_add_i32 s1, s0, 11
	s_cmp_ge_i32 s1, s12
	s_cbranch_scc1 .LBB0_1503
	s_getreg_b32 s2, hwreg(HW_REG_XCC_ID, 0, 4)
	v_readlane_b32 s0, v250, 4
	v_mov_b32 v1, s0
	s_waitcnt vmcnt(0)
	s_barrier
	s_cmp_eq_u32 s43, 1
	s_cbranch_scc0 .Learlyinv_10
	buffer_inv sc1
	s_waitcnt vmcnt(0)

.LBB0_1566:
	v_readlane_b32 s0, v255, 35
	s_add_i32 s22, s0, 12
	s_cmp_ge_i32 s22, s28
	s_cbranch_scc1 .LBB0_1620
	s_getreg_b32 s1, hwreg(HW_REG_XCC_ID, 0, 4)
	v_readlane_b32 s0, v250, 4
	v_mov_b32 v1, s0
	s_waitcnt vmcnt(0)
	s_waitcnt vmcnt(0)
	s_barrier
	s_cmp_eq_u32 s43, 1
	s_cbranch_scc0 .Learlyinv_11
	buffer_inv sc1
	s_waitcnt vmcnt(0)

.LBB0_1676:
	s_getreg_b32 s1, hwreg(HW_REG_XCC_ID, 0, 4)
	v_readlane_b32 s0, v250, 4
	v_mov_b32 v1, s0
	s_waitcnt vmcnt(0)
	s_waitcnt vmcnt(0)
	s_barrier
	s_cmp_eq_u32 s43, 1
	s_cbranch_scc0 .Learlyinv_12
	buffer_inv sc1
	s_waitcnt vmcnt(0)
.Learlyinv_12:
	s_mov_b64 s[4:5], exec
	v_readlane_b32 s2, v250, 2
	v_readlane_b32 s3, v250, 3
	s_and_b64 s[2:3], s[4:5], s[2:3]
	s_mov_b64 exec, s[2:3]
	s_cbranch_execnz .LBB0_1677
	s_getpc_b64 s[98:99]

.LBB0_1725:
	s_or_b64 exec, exec, s[8:9]
	s_mov_b64 s[2:3], exec
	v_mbcnt_lo_u32_b32 v0, s2, 0
	v_mbcnt_hi_u32_b32 v0, s3, v0
	v_cmp_eq_u32_e32 vcc, 0, v0
	s_waitcnt vmcnt(0)
	s_and_saveexec_b64 s[8:9], vcc
	s_cbranch_execnz .LBB0_1726
	s_getpc_b64 s[98:99]

.LBB0_1772:
	s_cmp_lt_i32 s21, 45
	s_cbranch_scc1 .LBB0_1826
	s_getreg_b32 s2, hwreg(HW_REG_XCC_ID, 0, 4)
	v_readlane_b32 s0, v250, 4
	v_mov_b32 v1, s0
	s_waitcnt vmcnt(0)
	s_barrier
	s_cmp_eq_u32 s43, 1
	s_cbranch_scc0 .Learlyinv_13
	buffer_inv sc1
	s_waitcnt vmcnt(0)
